# mlstm_D QK^T: branch ladder with per-MFMA ds_read waits replaced by straight-line double-buffered fragment reads
# speedup vs baseline: 1.0088x; 1.0088x over previous
; __device__ __forceinline__ void mlstm_D(LAS unsigned char* lds, int c, int h, const bf16_t* Z, const float* gi, const float* bcum, const float* marr, const bf16_t* CST, const float* NST,
;                                         const float* hgain, bf16_t* YCAT) {
;     ...
;     stage_tile<CH, DH, 8>(X, Z + (size_t)t0 * EVN + 2048 + h * DH, EVN, tid);
;     const int tl = 16 * wave + fr; const size_t trow = (size_t)(t0 + tl);
;     bf16x8 aq[8];
; #pragma unroll
;     for (int ks = 0; ks < 8; ++ks) aq[ks] = *(const bf16x8*)(Z + trow * EVN + 1024 + h * DH + 32 * ks + 8 * fq);
;     __syncthreads();
;     f32x4 S[8];
; #pragma unroll
;     for (int j = 0; j < 8; ++j) S[j] = (f32x4){0.f, 0.f, 0.f, 0.f};
.LBB0_576:
	s_or_b64 exec, exec, s[4:5]
	s_ashr_i32 s23, s15, 6
	s_mul_i32 s3, s14, 0x2800
	s_mul_hi_i32 s2, s14, 0x2800
	s_add_u32 s37, s30, s3
	v_add_u32_e32 v118, 0x200, v99
	s_addc_u32 s66, s31, s2
	s_lshl_b32 s24, s36, 9
	v_ashrrev_i32_e32 v122, 31, v99
	v_ashrrev_i32_e32 v124, 31, v118
	s_add_u32 s2, s37, s24
	v_lshrrev_b32_e32 v2, 27, v122
	v_lshrrev_b32_e32 v4, 27, v124
	s_addc_u32 s3, s66, 0
	v_add_u32_e32 v2, v99, v2
	v_add_u32_e32 v4, v118, v4
	s_add_u32 s2, s2, 0x1000
	v_ashrrev_i32_e32 v93, 5, v2
	v_and_b32_e32 v2, 0xffffffe0, v2
	v_ashrrev_i32_e32 v100, 5, v4
	v_and_b32_e32 v4, 0xffffffe0, v4
	v_add_u32_e32 v119, 0x400, v99
	v_add_u32_e32 v120, 0x600, v99
	s_addc_u32 s3, s3, 0
	v_sub_u32_e32 v92, v99, v2
	v_sub_u32_e32 v94, v118, v4
	v_ashrrev_i32_e32 v126, 31, v119
	v_ashrrev_i32_e32 v128, 31, v120
	v_mov_b64_e32 v[30:31], s[2:3]
	v_lshlrev_b32_e32 v74, 3, v92
	v_lshlrev_b32_e32 v76, 3, v94
	v_lshrrev_b32_e32 v10, 27, v126
	v_lshrrev_b32_e32 v12, 27, v128
	v_mad_i64_i32 v[2:3], s[2:3], v93, s68, v[30:31]
	v_ashrrev_i32_e32 v75, 31, v74
	v_mad_i64_i32 v[4:5], s[2:3], v100, s68, v[30:31]
	v_ashrrev_i32_e32 v77, 31, v76
	v_add_u32_e32 v10, v119, v10
	v_add_u32_e32 v12, v120, v12
	v_lshl_add_u64 v[2:3], v[74:75], 1, v[2:3]
	v_lshl_add_u64 v[6:7], v[76:77], 1, v[4:5]
	v_ashrrev_i32_e32 v101, 5, v10
	v_and_b32_e32 v10, 0xffffffe0, v10
	v_ashrrev_i32_e32 v102, 5, v12
	v_and_b32_e32 v12, 0xffffffe0, v12
	v_add_u32_e32 v123, 0x800, v99
	v_add_u32_e32 v125, 0xa00, v99
	v_add_u32_e32 v127, 0xc00, v99
	v_add_u32_e32 v129, 0xe00, v99
	global_load_dwordx4 v[2:5], v[2:3], off
	s_nop 0
	global_load_dwordx4 v[6:9], v[6:7], off
	v_sub_u32_e32 v98, v119, v10
	v_sub_u32_e32 v110, v120, v12
	v_ashrrev_i32_e32 v130, 31, v123
	v_ashrrev_i32_e32 v131, 31, v125
	v_ashrrev_i32_e32 v132, 31, v127
	v_ashrrev_i32_e32 v133, 31, v129
	v_lshlrev_b32_e32 v78, 3, v98
	v_lshlrev_b32_e32 v80, 3, v110
	v_lshrrev_b32_e32 v18, 27, v130
	v_lshrrev_b32_e32 v20, 27, v131
	v_lshrrev_b32_e32 v26, 27, v132
	v_lshrrev_b32_e32 v32, 27, v133
	v_and_b32_e32 v71, 15, v99
	v_mad_i64_i32 v[10:11], s[2:3], v101, s68, v[30:31]
	v_ashrrev_i32_e32 v79, 31, v78
	v_mad_i64_i32 v[12:13], s[2:3], v102, s68, v[30:31]
	v_ashrrev_i32_e32 v81, 31, v80
	v_add_u32_e32 v18, v123, v18
	v_add_u32_e32 v20, v125, v20
	v_add_u32_e32 v26, v127, v26
	v_add_u32_e32 v32, v129, v32
	v_lshl_add_u64 v[10:11], v[78:79], 1, v[10:11]
	v_lshl_add_u64 v[14:15], v[80:81], 1, v[12:13]
	v_ashrrev_i32_e32 v103, 5, v18
	v_and_b32_e32 v18, 0xffffffe0, v18
	v_ashrrev_i32_e32 v104, 5, v20
	v_and_b32_e32 v20, 0xffffffe0, v20
	v_ashrrev_i32_e32 v105, 5, v26
	v_and_b32_e32 v26, 0xffffffe0, v26
	v_ashrrev_i32_e32 v106, 5, v32
	v_and_b32_e32 v32, 0xffffffe0, v32
	v_lshl_or_b32 v135, s23, 4, v71
	global_load_dwordx4 v[10:13], v[10:11], off
	s_nop 0
	global_load_dwordx4 v[14:17], v[14:15], off
	v_sub_u32_e32 v111, v123, v18
	v_sub_u32_e32 v112, v125, v20
	v_sub_u32_e32 v113, v127, v26
	v_sub_u32_e32 v114, v129, v32
	v_add_u32_e32 v70, s14, v135
	v_lshlrev_b32_e32 v82, 3, v111
	v_lshlrev_b32_e32 v84, 3, v112
	v_lshlrev_b32_e32 v86, 3, v113
	v_lshlrev_b32_e32 v88, 3, v114
	v_mad_i64_i32 v[72:73], s[2:3], v70, s68, v[68:69]
	v_mad_i64_i32 v[18:19], s[2:3], v103, s68, v[30:31]
	v_ashrrev_i32_e32 v83, 31, v82
	v_mad_i64_i32 v[20:21], s[2:3], v104, s68, v[30:31]
	v_ashrrev_i32_e32 v85, 31, v84
	v_mad_i64_i32 v[26:27], s[2:3], v105, s68, v[30:31]
	v_ashrrev_i32_e32 v87, 31, v86
	v_mad_i64_i32 v[30:31], s[2:3], v106, s68, v[30:31]
	v_ashrrev_i32_e32 v89, 31, v88
	v_lshl_add_u64 v[34:35], v[72:73], 0, s[24:25]
	v_and_b32_e32 v66, 48, v99
	v_lshl_add_u64 v[18:19], v[82:83], 1, v[18:19]
	v_lshl_add_u64 v[22:23], v[84:85], 1, v[20:21]
	v_lshl_add_u64 v[26:27], v[86:87], 1, v[26:27]
	v_lshl_add_u64 v[30:31], v[88:89], 1, v[30:31]
	v_lshl_add_u64 v[90:91], v[34:35], 0, v[66:67]
	global_load_dwordx4 v[18:21], v[18:19], off
	s_nop 0
	global_load_dwordx4 v[22:25], v[22:23], off
	v_mul_lo_u32 v108, v93, s69
	global_load_dwordx4 v[26:29], v[26:27], off
	v_lshlrev_b32_e32 v107, 4, v92
	global_load_dwordx4 v[30:33], v[30:31], off
	s_nop 0
	global_load_dwordx4 v[62:65], v[90:91], off offset:2048
	global_load_dwordx4 v[58:61], v[90:91], off offset:2112
	global_load_dwordx4 v[54:57], v[90:91], off offset:2176
	global_load_dwordx4 v[50:53], v[90:91], off offset:2240
	global_load_dwordx4 v[46:49], v[90:91], off offset:2304
	global_load_dwordx4 v[42:45], v[90:91], off offset:2368
	global_load_dwordx4 v[38:41], v[90:91], off offset:2432
	global_load_dwordx4 v[34:37], v[90:91], off offset:2496
	v_add3_u32 v92, s51, v108, v107
	v_lshlrev_b32_e32 v108, 4, v94
	v_lshlrev_b32_e32 v109, 4, v98
	v_lshlrev_b32_e32 v110, 4, v110
	v_lshlrev_b32_e32 v111, 4, v111
	v_lshlrev_b32_e32 v112, 4, v112
	v_lshlrev_b32_e32 v113, 4, v113
	s_waitcnt vmcnt(15)
	ds_write_b128 v92, v[2:5]
	v_mul_lo_u32 v2, v100, s69
	v_add3_u32 v2, s51, v2, v108
	s_waitcnt vmcnt(14)
	ds_write_b128 v2, v[6:9]
	v_mul_lo_u32 v2, v101, s69
	v_add3_u32 v2, s51, v2, v109
	v_lshlrev_b32_e32 v114, 4, v114
	v_add_u32_e32 v121, s51, v66
	s_cmp_gt_i32 s23, -1
	s_cselect_b64 s[4:5], -1, 0
	s_cmp_lt_i32 s23, 0
	v_mad_u32_u24 v92, v71, s69, v121
	s_waitcnt vmcnt(13)
	ds_write_b128 v2, v[10:13]
	v_mul_lo_u32 v2, v102, s69
	v_add3_u32 v2, s51, v2, v110
	s_waitcnt vmcnt(12)
	ds_write_b128 v2, v[14:17]
	v_mul_lo_u32 v2, v103, s69
	v_add3_u32 v2, s51, v2, v111
	s_waitcnt vmcnt(11)
	ds_write_b128 v2, v[18:21]
	v_mul_lo_u32 v2, v104, s69
	v_add3_u32 v2, s51, v2, v112
	s_waitcnt vmcnt(10)
	ds_write_b128 v2, v[22:25]
	v_mul_lo_u32 v2, v105, s69
	v_add3_u32 v2, s51, v2, v113
	s_waitcnt vmcnt(9)
	ds_write_b128 v2, v[26:29]
	v_mul_lo_u32 v2, v106, s69
	v_add3_u32 v2, s51, v2, v114
	s_waitcnt vmcnt(8)
	ds_write_b128 v2, v[30:33]
	v_mov_b32_e32 v30, v67
	v_mov_b32_e32 v31, v67
	v_mov_b32_e32 v32, v67
	v_mov_b32_e32 v33, v67
	s_waitcnt lgkmcnt(0)
	s_barrier
; #define MFMA16(b, a, c) __builtin_amdgcn_mfma_f32_16x16x32_bf16((b), (a), (c), 0, 0, 0)
; __device__ __forceinline__ void mlstm_D(LAS unsigned char* lds, int c, int h, const bf16_t* Z, const float* gi, const float* bcum, const float* marr, const bf16_t* CST, const float* NST,
;                                         const float* hgain, bf16_t* YCAT) {
;     ...
;     for (int ks = 0; ks < 8; ++ks)
;         {
; #pragma unroll
;           for (int j = 0; j < 8; ++j) if (j <= wave) S[j] = MFMA16(row_frag(X, (DH + 8) * 2, 16 * j, 32 * ks, lane), aq[ks], S[j]);
;           asm volatile("" ::: "memory"); }
	ds_read_b128 v[136:139], v92
	ds_read_b128 v[140:143], v92 offset:8448
	ds_read_b128 v[144:147], v92 offset:16896
	ds_read_b128 v[148:151], v92 offset:25344
	ds_read_b128 v[152:155], v92 offset:33792
	ds_read_b128 v[156:159], v92 offset:42240
	ds_read_b128 v[160:163], v92 offset:50688
	ds_read_b128 v[164:167], v92 offset:59136
	ds_read_b128 v[168:171], v92 offset:64
	ds_read_b128 v[172:175], v92 offset:8512
	ds_read_b128 v[176:179], v92 offset:16960
	ds_read_b128 v[180:183], v92 offset:25408
	ds_read_b128 v[184:187], v92 offset:33856
	ds_read_b128 v[188:191], v92 offset:42304
	ds_read_b128 v[192:195], v92 offset:50752
	ds_read_b128 v[196:199], v92 offset:59200
	s_waitcnt vmcnt(7) lgkmcnt(8)
	v_mfma_f32_16x16x32_bf16 v[30:33], v[136:139], v[62:65], 0
	v_mfma_f32_16x16x32_bf16 v[26:29], v[140:143], v[62:65], 0
	v_mfma_f32_16x16x32_bf16 v[22:25], v[144:147], v[62:65], 0
	v_mfma_f32_16x16x32_bf16 v[18:21], v[148:151], v[62:65], 0
	v_mfma_f32_16x16x32_bf16 v[14:17], v[152:155], v[62:65], 0
	v_mfma_f32_16x16x32_bf16 v[10:13], v[156:159], v[62:65], 0
	v_mfma_f32_16x16x32_bf16 v[6:9], v[160:163], v[62:65], 0
	v_mfma_f32_16x16x32_bf16 v[2:5], v[164:167], v[62:65], 0
	ds_read_b128 v[136:139], v92 offset:128
	ds_read_b128 v[140:143], v92 offset:8576
	ds_read_b128 v[144:147], v92 offset:17024
	ds_read_b128 v[148:151], v92 offset:25472
	ds_read_b128 v[152:155], v92 offset:33920
	ds_read_b128 v[156:159], v92 offset:42368
	ds_read_b128 v[160:163], v92 offset:50816
	ds_read_b128 v[164:167], v92 offset:59264
	s_waitcnt vmcnt(6) lgkmcnt(8)
	v_mfma_f32_16x16x32_bf16 v[30:33], v[168:171], v[58:61], v[30:33]
	v_mfma_f32_16x16x32_bf16 v[26:29], v[172:175], v[58:61], v[26:29]
	v_mfma_f32_16x16x32_bf16 v[22:25], v[176:179], v[58:61], v[22:25]
	v_mfma_f32_16x16x32_bf16 v[18:21], v[180:183], v[58:61], v[18:21]
	v_mfma_f32_16x16x32_bf16 v[14:17], v[184:187], v[58:61], v[14:17]
	v_mfma_f32_16x16x32_bf16 v[10:13], v[188:191], v[58:61], v[10:13]
	v_mfma_f32_16x16x32_bf16 v[6:9], v[192:195], v[58:61], v[6:9]
	v_mfma_f32_16x16x32_bf16 v[2:5], v[196:199], v[58:61], v[2:5]
	ds_read_b128 v[168:171], v92 offset:192
	ds_read_b128 v[172:175], v92 offset:8640
	ds_read_b128 v[176:179], v92 offset:17088
	ds_read_b128 v[180:183], v92 offset:25536
	ds_read_b128 v[184:187], v92 offset:33984
	ds_read_b128 v[188:191], v92 offset:42432
	ds_read_b128 v[192:195], v92 offset:50880
	ds_read_b128 v[196:199], v92 offset:59328
	s_waitcnt vmcnt(5) lgkmcnt(8)
	v_mfma_f32_16x16x32_bf16 v[30:33], v[136:139], v[54:57], v[30:33]
	v_mfma_f32_16x16x32_bf16 v[26:29], v[140:143], v[54:57], v[26:29]
	v_mfma_f32_16x16x32_bf16 v[22:25], v[144:147], v[54:57], v[22:25]
	v_mfma_f32_16x16x32_bf16 v[18:21], v[148:151], v[54:57], v[18:21]
	v_mfma_f32_16x16x32_bf16 v[14:17], v[152:155], v[54:57], v[14:17]
	v_mfma_f32_16x16x32_bf16 v[10:13], v[156:159], v[54:57], v[10:13]
	v_mfma_f32_16x16x32_bf16 v[6:9], v[160:163], v[54:57], v[6:9]
	v_mfma_f32_16x16x32_bf16 v[2:5], v[164:167], v[54:57], v[2:5]
	ds_read_b128 v[136:139], v92 offset:256
	ds_read_b128 v[140:143], v92 offset:8704
	ds_read_b128 v[144:147], v92 offset:17152
	ds_read_b128 v[148:151], v92 offset:25600
	ds_read_b128 v[152:155], v92 offset:34048
	ds_read_b128 v[156:159], v92 offset:42496
	ds_read_b128 v[160:163], v92 offset:50944
	ds_read_b128 v[164:167], v92 offset:59392
	s_waitcnt vmcnt(4) lgkmcnt(8)
; #define MFMA16(b, a, c) __builtin_amdgcn_mfma_f32_16x16x32_bf16((b), (a), (c), 0, 0, 0)
; __device__ __forceinline__ void mlstm_D(LAS unsigned char* lds, int c, int h, const bf16_t* Z, const float* gi, const float* bcum, const float* marr, const bf16_t* CST, const float* NST,
;                                         const float* hgain, bf16_t* YCAT) {
;     ...
;     for (int ks = 0; ks < 8; ++ks)
;         {
; #pragma unroll
;           for (int j = 0; j < 8; ++j) if (j <= wave) S[j] = MFMA16(row_frag(X, (DH + 8) * 2, 16 * j, 32 * ks, lane), aq[ks], S[j]);
;           asm volatile("" ::: "memory"); }
	v_mfma_f32_16x16x32_bf16 v[30:33], v[168:171], v[50:53], v[30:33]
	v_mfma_f32_16x16x32_bf16 v[26:29], v[172:175], v[50:53], v[26:29]
	v_mfma_f32_16x16x32_bf16 v[22:25], v[176:179], v[50:53], v[22:25]
	v_mfma_f32_16x16x32_bf16 v[18:21], v[180:183], v[50:53], v[18:21]
	v_mfma_f32_16x16x32_bf16 v[14:17], v[184:187], v[50:53], v[14:17]
	v_mfma_f32_16x16x32_bf16 v[10:13], v[188:191], v[50:53], v[10:13]
	v_mfma_f32_16x16x32_bf16 v[6:9], v[192:195], v[50:53], v[6:9]
	v_mfma_f32_16x16x32_bf16 v[2:5], v[196:199], v[50:53], v[2:5]
	ds_read_b128 v[168:171], v92 offset:320
	ds_read_b128 v[172:175], v92 offset:8768
	ds_read_b128 v[176:179], v92 offset:17216
	ds_read_b128 v[180:183], v92 offset:25664
	ds_read_b128 v[184:187], v92 offset:34112
	ds_read_b128 v[188:191], v92 offset:42560
	ds_read_b128 v[192:195], v92 offset:51008
	ds_read_b128 v[196:199], v92 offset:59456
	s_waitcnt vmcnt(3) lgkmcnt(8)
	v_mfma_f32_16x16x32_bf16 v[30:33], v[136:139], v[46:49], v[30:33]
	v_mfma_f32_16x16x32_bf16 v[26:29], v[140:143], v[46:49], v[26:29]
	v_mfma_f32_16x16x32_bf16 v[22:25], v[144:147], v[46:49], v[22:25]
	v_mfma_f32_16x16x32_bf16 v[18:21], v[148:151], v[46:49], v[18:21]
	v_mfma_f32_16x16x32_bf16 v[14:17], v[152:155], v[46:49], v[14:17]
	v_mfma_f32_16x16x32_bf16 v[10:13], v[156:159], v[46:49], v[10:13]
	v_mfma_f32_16x16x32_bf16 v[6:9], v[160:163], v[46:49], v[6:9]
	v_mfma_f32_16x16x32_bf16 v[2:5], v[164:167], v[46:49], v[2:5]
	ds_read_b128 v[136:139], v92 offset:384
	ds_read_b128 v[140:143], v92 offset:8832
	ds_read_b128 v[144:147], v92 offset:17280
	ds_read_b128 v[148:151], v92 offset:25728
	ds_read_b128 v[152:155], v92 offset:34176
	ds_read_b128 v[156:159], v92 offset:42624
	ds_read_b128 v[160:163], v92 offset:51072
	ds_read_b128 v[164:167], v92 offset:59520
	s_waitcnt vmcnt(2) lgkmcnt(8)
	v_mfma_f32_16x16x32_bf16 v[30:33], v[168:171], v[42:45], v[30:33]
	v_mfma_f32_16x16x32_bf16 v[26:29], v[172:175], v[42:45], v[26:29]
	v_mfma_f32_16x16x32_bf16 v[22:25], v[176:179], v[42:45], v[22:25]
	v_mfma_f32_16x16x32_bf16 v[18:21], v[180:183], v[42:45], v[18:21]
	v_mfma_f32_16x16x32_bf16 v[14:17], v[184:187], v[42:45], v[14:17]
	v_mfma_f32_16x16x32_bf16 v[10:13], v[188:191], v[42:45], v[10:13]
	v_mfma_f32_16x16x32_bf16 v[6:9], v[192:195], v[42:45], v[6:9]
	v_mfma_f32_16x16x32_bf16 v[2:5], v[196:199], v[42:45], v[2:5]
	ds_read_b128 v[168:171], v92 offset:448
	ds_read_b128 v[172:175], v92 offset:8896
	ds_read_b128 v[176:179], v92 offset:17344
	ds_read_b128 v[180:183], v92 offset:25792
	ds_read_b128 v[184:187], v92 offset:34240
	ds_read_b128 v[188:191], v92 offset:42688
	ds_read_b128 v[192:195], v92 offset:51136
	ds_read_b128 v[196:199], v92 offset:59584
	s_waitcnt vmcnt(1) lgkmcnt(8)
	v_mfma_f32_16x16x32_bf16 v[30:33], v[136:139], v[38:41], v[30:33]
	v_mfma_f32_16x16x32_bf16 v[26:29], v[140:143], v[38:41], v[26:29]
	v_mfma_f32_16x16x32_bf16 v[22:25], v[144:147], v[38:41], v[22:25]
	v_mfma_f32_16x16x32_bf16 v[18:21], v[148:151], v[38:41], v[18:21]
	v_mfma_f32_16x16x32_bf16 v[14:17], v[152:155], v[38:41], v[14:17]
	v_mfma_f32_16x16x32_bf16 v[10:13], v[156:159], v[38:41], v[10:13]
	v_mfma_f32_16x16x32_bf16 v[6:9], v[160:163], v[38:41], v[6:9]
	v_mfma_f32_16x16x32_bf16 v[2:5], v[164:167], v[38:41], v[2:5]
	s_waitcnt vmcnt(0) lgkmcnt(0)
	v_mfma_f32_16x16x32_bf16 v[30:33], v[168:171], v[34:37], v[30:33]
	v_mfma_f32_16x16x32_bf16 v[26:29], v[172:175], v[34:37], v[26:29]
	v_mfma_f32_16x16x32_bf16 v[22:25], v[176:179], v[34:37], v[22:25]
	v_mfma_f32_16x16x32_bf16 v[18:21], v[180:183], v[34:37], v[18:21]
	v_mfma_f32_16x16x32_bf16 v[14:17], v[184:187], v[34:37], v[14:17]
	v_mfma_f32_16x16x32_bf16 v[10:13], v[188:191], v[34:37], v[10:13]
	v_mfma_f32_16x16x32_bf16 v[6:9], v[192:195], v[34:37], v[6:9]
	v_mfma_f32_16x16x32_bf16 v[2:5], v[196:199], v[34:37], v[2:5]
